# work re-balancing: in-proj tail-fill 7 conversion steps (was 6), layer-1 attention-phase quota 19 (was 20)
# speedup vs baseline: 1.0002x; 1.0002x over previous
; #define LAS __attribute__((address_space(3)))
; #define PHASE_BEGIN() Ctx c = c0; { int t_ = c0.tid; asm volatile("" : "+v"(t_)); c.tid = t_; c.lane = t_ & 63; c.wave = __builtin_amdgcn_readfirstlane(t_ >> 6); } \
;     GAS unsigned char* wsb = (GAS unsigned char*)a.ws; asm volatile("" : "+s"(wsb));
; #define SEAM(k) do { if (IN(k) && IN((k) + 1)) { XcdBarrier b_ = bar; { GAS unsigned* t_ = (GAS unsigned*)b_.bar; asm volatile("" : "+s"(t_)); b_.bar = (unsigned*)t_; } xcd_barrier(b_); } } while (0)
; __device__ __forceinline__ void bg_take(const Args& a, const Ctx& c0, int n) {
;     PHASE_BEGIN();
;     unsigned* head = WSP(unsigned, WS_CTL) + CW_QHEAD;
;     volatile LAS unsigned* bc = (volatile LAS unsigned*)(c.lds + LDS_MISC + 64);
;     LAS float* scr = (LAS float*)(c.lds + c.wave * 16640);
;     __syncthreads();
;     for (int i = 0; i < n; ++i) {
;         if (c.tid == 0) { unsigned s = __hip_atomic_fetch_add(head, 1u, __ATOMIC_RELAXED, __HIP_MEMORY_SCOPE_AGENT); if (s >= (unsigned)BG_STEPS) s = 0xffffffffu; bc[0] = s; }
;         __syncthreads();
;         const unsigned s = bc[0];
;         if (s == 0xffffffffu) break;
;         const int g = (int)s * 8 + c.wave;
;         if (g < T_MOE) convert_tile(a, wsb, 0, T_SMALL + g, scr, c.lane); else convert_tile(a, wsb, 1, g - T_MOE, scr, c.lane);
;         __syncthreads();
;     }
; __global__ void __launch_bounds__(512, 2) mk_fwd(Args a) {
;     ...
;         if (IN(pb + 1)) bg_fill(a, c, l * 8 + 1, 0);
;     ...
;         SEAM(pb + 1);
.LBB0_322:
	v_readlane_b32 s2, v255, 42
	s_nop 3
	s_cmp_lg_u32 s2, 0
	s_cbranch_scc1 .LtailA_ret
	s_cmp_lt_u32 s90, 48
	s_cbranch_scc1 .LtailA_cont
	v_writelane_b32 v255, 1, 42
	s_mov_b32 s30, 0xc3e00000
	s_movk_i32 s78, 0x315c
	v_readlane_b32 s76, v254, 53
	s_mov_b32 s81, 0x10000
	s_mov_b32 s82, 0x18000
	s_mov_b32 s83, 0x8000
	s_mov_b32 s86, 0xc000
	s_mov_b32 s14, 7
	s_branch .Lbt1_entry

; __device__ __forceinline__ void bg_take(const Args& a, const Ctx& c0, int n) {
;     ...
;     for (int i = 0; i < n; ++i) {
;         if (c.tid == 0) { unsigned s = __hip_atomic_fetch_add(head, 1u, __ATOMIC_RELAXED, __HIP_MEMORY_SCOPE_AGENT); if (s >= (unsigned)BG_STEPS) s = 0xffffffffu; bc[0] = s; }
;         __syncthreads();
;         const unsigned s = bc[0];
;         if (s == 0xffffffffu) break;
;         const int g = (int)s * 8 + c.wave;
;         if (g < T_MOE) convert_tile(a, wsb, 0, T_SMALL + g, scr, c.lane); else convert_tile(a, wsb, 1, g - T_MOE, scr, c.lane);
;         __syncthreads();
;     }
; __global__ void __launch_bounds__(512, 2) mk_fwd(Args a) {
;     ...
;         if (IN(pb + 5) && (c.bid & 1) == 0) { if (l == 0) mod_items(a, c, 1); bg_take(a, c, l == 0 ? 26 : 24); }
.Lbal1_l1:
	s_mov_b32 s14, 19

; __device__ __forceinline__ void bg_take(const Args& a, const Ctx& c0, int n) {
;     ...
;     for (int i = 0; i < n; ++i) {
;         if (c.tid == 0) { unsigned s = __hip_atomic_fetch_add(head, 1u, __ATOMIC_RELAXED, __HIP_MEMORY_SCOPE_AGENT); if (s >= (unsigned)BG_STEPS) s = 0xffffffffu; bc[0] = s; }
;         __syncthreads();
;         const unsigned s = bc[0];
;         if (s == 0xffffffffu) break;
;         const int g = (int)s * 8 + c.wave;
;         if (g < T_MOE) convert_tile(a, wsb, 0, T_SMALL + g, scr, c.lane); else convert_tile(a, wsb, 1, g - T_MOE, scr, c.lane);
;         __syncthreads();
;     }
; __global__ void __launch_bounds__(512, 2) mk_fwd(Args a) {
;     ...
;         if (IN(pb + 5) && (c.bid & 1) == 1) { bg_take(a, c, l == 0 ? 26 : 24); if (l == 0) mod_items(a, c, 1); }
.Lbal2_l1:
	s_mov_b32 s10, 19
